# v64 + the padding-row redirect also for each workgroup's first down-projection unit (offsets computed in the prologue)
# speedup vs baseline: 1.0098x; 1.0038x over previous
.LBB0_1029:
	v_bfe_i32 v2, v4, 27, 1
	v_lshlrev_b32_e32 v0, 4, v4
	v_lshrrev_b32_e32 v2, 22, v2
	v_add_u32_e32 v2, v0, v2
	v_and_b32_e32 v2, 0xfffffc00, v2
	v_sub_u32_e32 v2, v0, v2
	v_ashrrev_i32_e32 v1, 31, v4
	v_lshrrev_b32_e32 v3, 4, v2
	v_lshrrev_b32_e32 v1, 26, v1
	v_bitop3_b32 v3, v3, v2, 32 bitop3:0x6c
	v_ashrrev_i32_e32 v2, 31, v2
	v_add_u32_e32 v1, v4, v1
	v_lshrrev_b32_e32 v2, 26, v2
	v_ashrrev_i32_e32 v1, 6, v1
	v_add_u32_e32 v2, v3, v2
	s_add_u32 s21, s90, 0x4a800000
	v_lshlrev_b32_e32 v5, 3, v1
	v_ashrrev_i32_e32 v2, 6, v2
	s_addc_u32 s33, s91, 0
	v_and_b32_e32 v5, -16, v5
	v_mul_i32_i24_e32 v6, 64, v2
	s_add_u32 s6, s90, 0x14800000
	v_readlane_b32 s10, v255, 25
	v_add_u32_e32 v5, v2, v5
	v_sub_u32_e32 v3, v3, v6
	v_mov_b32_e32 v159, 1
	s_addc_u32 s7, s91, 0
	s_lshr_b32 s18, s10, 8
	v_lshlrev_b32_e32 v1, 5, v1
	v_ashrrev_i16_sdwa v3, v159, sext(v3) dst_sel:DWORD dst_unused:UNUSED_PAD src0_sel:DWORD src1_sel:BYTE_0
	v_lshlrev_b32_e32 v6, 1, v5
	v_lshrrev_b32_e32 v7, 2, v5
	v_and_b32_e32 v2, 3, v2
	s_mov_b32 s10, 0x1fffe0
	v_and_b32_e32 v1, 32, v1
	v_bfe_i32 v3, v3, 0, 16
	v_and_b32_e32 v6, 24, v6
	v_and_b32_e32 v7, 4, v7
	v_and_or_b32 v2, v5, s10, v2
	v_or3_b32 v2, v2, v7, v6
	v_add_lshl_u32 v1, v1, v3, 1
	v_add_u32_e32 v0, 0x2000, v0
	v_lshl_add_u32 v148, v2, 11, v1
	v_ashrrev_i32_e32 v1, 31, v0
	v_lshrrev_b32_e32 v1, 22, v1
	v_add_u32_e32 v1, v0, v1
	v_ashrrev_i32_e32 v1, 10, v1
	v_mul_i32_i24_e32 v2, 0x400, v1
	v_sub_u32_e32 v0, v0, v2
	v_lshrrev_b32_e32 v2, 4, v0
	v_bitop3_b32 v0, v2, v0, 32 bitop3:0x6c
	v_ashrrev_i32_e32 v3, 31, v0
	v_lshrrev_b32_e32 v3, 26, v3
	v_lshlrev_b32_e32 v2, 3, v1
	v_add_u32_e32 v3, v0, v3
	v_lshlrev_b32_e32 v1, 5, v1
	v_and_b32_e32 v6, 32, v1
	v_and_b32_e32 v1, 0xc0, v3
	v_and_b32_e32 v2, -16, v2
	v_ashrrev_i32_e32 v5, 6, v3
	v_sub_u32_e32 v0, v0, v1
	v_add_u32_e32 v2, v5, v2
	v_ashrrev_i16_sdwa v0, v159, sext(v0) dst_sel:DWORD dst_unused:UNUSED_PAD src0_sel:DWORD src1_sel:BYTE_0
	v_and_b32_e32 v5, 3, v5
	v_bfe_i32 v3, v0, 0, 16
	v_lshlrev_b32_e32 v0, 1, v2
	v_lshrrev_b32_e32 v1, 2, v2
	v_and_or_b32 v2, v2, s10, v5
	s_lshl_b32 s10, s0, 2
	s_add_i32 s10, s10, 0
	s_add_i32 s10, s10, 0x20400
	v_and_b32_e32 v0, 24, v0
	v_and_b32_e32 v1, 4, v1
	v_mov_b32_e32 v5, s10
	v_or3_b32 v2, v2, v1, v0
	ds_read2_b32 v[0:1], v5 offset0:32 offset1:64
	ds_read_b32 v100, v5
	v_add_lshl_u32 v3, v6, v3, 1
	v_lshl_add_u32 v150, v2, 11, v3
	ds_read_b32 v2, v5 offset:384
	s_lshl_b32 s48, s94, 10
	s_waitcnt lgkmcnt(1)
	v_readfirstlane_b32 s10, v0
	s_abs_i32 s11, s10
	v_cvt_f32_u32_e32 v0, s11
	s_waitcnt lgkmcnt(0)
	v_readfirstlane_b32 s12, v2
	v_readfirstlane_b32 s99, v100
	s_sub_i32 s14, 0, s11
	s_lshl_b32 s12, s12, 3
	v_rcp_iflag_f32_e32 v0, v0
	s_sub_i32 s1, s1, s12
	s_ashr_i32 s13, s1, 31
	s_abs_i32 s1, s1
	v_mul_f32_e32 v0, 0x4f7ffffe, v0
	v_cvt_u32_f32_e32 v0, v0
	s_ashr_i32 s10, s10, 31
	s_xor_b32 s10, s13, s10
	v_readfirstlane_b32 s12, v1
	v_readfirstlane_b32 s15, v0
	s_mul_i32 s14, s14, s15
	s_mul_hi_u32 s14, s15, s14
	s_add_i32 s15, s15, s14
	s_mul_hi_u32 s14, s1, s15
	s_mul_i32 s15, s14, s11
	s_sub_i32 s1, s1, s15
	s_add_i32 s15, s14, 1
	s_sub_i32 s16, s1, s11
	s_cmp_ge_u32 s1, s11
	s_cselect_b32 s14, s15, s14
	s_cselect_b32 s1, s16, s1
	s_add_i32 s15, s14, 1
	s_sub_i32 s16, s1, s11
	s_cmp_ge_u32 s1, s11
	s_cselect_b32 s1, s16, s1
	s_cselect_b32 s11, s15, s14
	s_xor_b32 s1, s1, s13
	s_sub_i32 s1, s1, s13
	s_lshl_b32 s1, s1, 8
	s_xor_b32 s11, s11, s10
	s_add_i32 s49, s1, s12
	s_sub_i32 s99, s99, s1
	s_ashr_i32 s1, s0, 31
	s_sub_i32 s10, s11, s10
	s_lshl_b64 s[12:13], s[0:1], 22
	s_add_u32 s1, s21, s12
	s_addc_u32 s14, s33, s13
	s_ashr_i32 s11, s10, 31
	s_lshl_b64 s[12:13], s[10:11], 19
	s_add_u32 s12, s1, s12
	v_mbcnt_lo_u32_b32 v0, -1, 0
	v_mbcnt_hi_u32_b32 v0, -1, v0
	v_readlane_b32 s1, v255, 4
	s_addc_u32 s13, s14, s13
	s_mov_b64 s[14:15], s[12:13]
	v_add_u32_e32 v0, s1, v0
	s_add_i32 s1, s49, 0x80
	v_ashrrev_i32_e32 v2, 31, v0
	v_lshrrev_b32_e32 v2, 26, v2
	v_lshlrev_b32_e32 v1, 4, v0
	v_add_u32_e32 v2, v0, v2
	v_bfe_i32 v0, v0, 27, 1
	v_lshrrev_b32_e32 v0, 22, v0
	v_add_u32_e32 v0, v1, v0
	v_and_b32_e32 v0, 0xfffffc00, v0
	v_sub_u32_e32 v0, v1, v0
	v_lshrrev_b32_e32 v3, 4, v0
	v_bitop3_b32 v3, v3, v0, 32 bitop3:0x6c
	v_ashrrev_i32_e32 v0, 31, v0
	v_ashrrev_i32_e32 v2, 6, v2
	v_lshrrev_b32_e32 v0, 26, v0
	v_lshlrev_b32_e32 v5, 3, v2
	v_add_u32_e32 v0, v3, v0
	v_and_b32_e32 v5, -16, v5
	v_ashrrev_i32_e32 v0, 6, v0
	v_add_u32_e32 v5, v0, v5
	v_mul_i32_i24_e32 v0, 64, v0
	v_sub_u32_e32 v0, v3, v0
	v_lshlrev_b32_e32 v2, 5, v2
	v_ashrrev_i16_sdwa v0, v159, sext(v0) dst_sel:DWORD dst_unused:UNUSED_PAD src0_sel:DWORD src1_sel:BYTE_0
	v_and_b32_e32 v2, 32, v2
	v_bfe_i32 v0, v0, 0, 16
	v_add_lshl_u32 v2, v2, v0, 1
	v_cmp_gt_u32_e32 vcc, s99, v5
	s_nop 1
	v_cndmask_b32_e32 v0, 0, v5, vcc
	v_add_u32_e32 v0, s49, v0
	v_add_u32_e32 v3, 0x80, v5
	v_cmp_gt_u32_e32 vcc, s99, v3
	s_nop 1
	v_cndmask_b32_e32 v3, 0, v3, vcc
	v_add_u32_e32 v3, s49, v3
	v_add_u32_e32 v1, 0x2000, v1
	v_lshl_add_u32 v0, v0, 11, v2
	v_lshl_add_u32 v2, v3, 11, v2
	v_ashrrev_i32_e32 v3, 31, v1
	v_lshrrev_b32_e32 v3, 22, v3
	v_add_u32_e32 v3, v1, v3
	v_ashrrev_i32_e32 v3, 10, v3
	v_mul_i32_i24_e32 v5, 0x400, v3
	v_sub_u32_e32 v1, v1, v5
	v_lshrrev_b32_e32 v5, 4, v1
	v_bitop3_b32 v1, v5, v1, 32 bitop3:0x6c
	v_ashrrev_i32_e32 v6, 31, v1
	v_lshrrev_b32_e32 v6, 26, v6
	v_add_u32_e32 v6, v1, v6
	v_ashrrev_i32_e32 v7, 6, v6
	v_and_b32_e32 v6, 0xc0, v6
	v_lshlrev_b32_e32 v5, 3, v3
	v_sub_u32_e32 v1, v1, v6
	v_and_b32_e32 v5, -16, v5
	v_lshlrev_b32_e32 v3, 5, v3
	v_ashrrev_i16_sdwa v1, v159, sext(v1) dst_sel:DWORD dst_unused:UNUSED_PAD src0_sel:DWORD src1_sel:BYTE_0
	v_add_u32_e32 v5, v7, v5
	v_and_b32_e32 v3, 32, v3
	v_bfe_i32 v1, v1, 0, 16
	v_add_lshl_u32 v1, v3, v1, 1
	v_cmp_gt_u32_e32 vcc, s99, v5
	s_nop 1
	v_cndmask_b32_e32 v3, 0, v5, vcc
	v_add_u32_e32 v3, s49, v3
	v_lshl_add_u32 v152, v3, 11, v1
	v_add_u32_e32 v3, 0x80, v5
	v_cmp_gt_u32_e32 vcc, s99, v3
	s_nop 1
	v_cndmask_b32_e32 v3, 0, v3, vcc
	v_add_u32_e32 v3, s49, v3
	s_add_i32 s1, s48, 0
	s_add_i32 m0, s1, 0x10000
	v_lshl_add_u32 v3, v3, 11, v1
	global_load_lds_dwordx4 v148, s[14:15]
	s_add_i32 m0, s1, 0x12000
	v_mov_b32_e32 v149, 0
	global_load_lds_dwordx4 v150, s[14:15]
	s_add_u32 s14, s12, 0x40000
	s_addc_u32 s15, s13, 0
	s_add_i32 m0, s1, 0x14000
	s_add_i32 s11, s1, 0x2000
	global_load_lds_dwordx4 v148, s[14:15]
	s_add_i32 m0, s1, 0x16000
	s_add_i32 s50, s1, 0x4000
	global_load_lds_dwordx4 v150, s[14:15]
	s_mov_b64 s[14:15], s[6:7]
	s_mov_b32 m0, s1
	s_add_i32 s51, s1, 0x6000
	global_load_lds_dwordx4 v0, s[14:15]
	s_mov_b32 m0, s11
	s_cmp_eq_u32 s18, 1
	global_load_lds_dwordx4 v152, s[14:15]
	s_mov_b64 s[14:15], s[6:7]
	s_mov_b32 m0, s50
	s_mov_b32 s66, s60
	global_load_lds_dwordx4 v2, s[14:15]
	s_mov_b32 m0, s51
	s_mov_b32 s54, 0
	global_load_lds_dwordx4 v3, s[14:15]
	s_mov_b32 s52, 0x10000
	v_mov_b32_e32 v151, v149
	v_mov_b32_e32 v1, v149
	s_cselect_b64 s[14:15], -1, 0
	s_cmp_lg_u32 s18, 1
	v_mov_b32_e32 v153, v149
	s_cbranch_scc1 .LBB0_1031
	s_barrier
